# strategy 4: one static s_setprio 1 for waves 4-7 while the workgroup runs its attention units, reset at the SGU unit (timing only)
# baseline (speedup 1.0000x reference)
.LBB0_400:
	s_mov_b64 s[8:9], -1
	s_and_b64 vcc, exec, s[6:7]
	s_cbranch_vccz .LBB0_393
	s_cmp_lt_u32 s67, 0x100
	s_cbranch_scc1 .Lap_skip
	s_setprio 1
.Lap_skip:
	s_mov_b64 s[6:7], s[0:1]
	s_load_dwordx2 s[14:15], s[6:7], 0xd0
	s_ashr_i32 s18, s4, 3
	v_mbcnt_lo_u32_b32 v0, -1, 0
	v_mbcnt_hi_u32_b32 v0, -1, v0
	s_ashr_i32 s19, s18, 31
	v_add_u32_e32 v8, s67, v0
	s_lshl_b64 s[16:17], s[18:19], 11
	v_lshlrev_b32_e32 v2, 2, v8
	v_ashrrev_i32_e32 v3, 31, v2
	v_lshl_add_u64 v[4:5], s[16:17], 0, v[2:3]
	s_and_b32 s23, s4, 7
	v_lshlrev_b64 v[4:5], 5, v[4:5]
	s_waitcnt lgkmcnt(0)
	v_lshl_add_u64 v[4:5], s[14:15], 0, v[4:5]
	s_lshl_b32 s52, s23, 2
	v_lshl_add_u64 v[4:5], v[4:5], 0, s[52:53]
	s_mov_b64 s[4:5], 0x100000
	v_lshl_add_u64 v[6:7], v[4:5], 0, s[4:5]
	s_mov_b32 s4, 0x100000
	v_add_co_u32_e32 v4, vcc, s4, v4
	v_and_b32_e32 v9, 64, v234
	s_nop 0
	v_addc_co_u32_e32 v5, vcc, 0, v5, vcc
	global_load_dword v4, v[4:5], off
	s_nop 0
	global_load_dword v0, v[6:7], off offset:32
	global_load_dword v3, v[6:7], off offset:64
	s_nop 0
	global_load_dword v7, v[6:7], off offset:96
	s_lshl_b32 s100, s18, 2
	s_add_u32 s100, s100, s12
	s_addc_u32 s101, s13, 0
	s_add_u32 s100, s100, s14
	s_addc_u32 s101, s101, s15
	v_mov_b32_e32 v241, 0x20000
	global_load_dword v240, v241, s[100:101] sc1
	v_add_u32_e32 v5, -1, v234
	s_lshl_b32 s100, s25, 9
	s_add_i32 s100, s100, s67
	v_and_b32_e32 v56, 31, v234
	v_or_b32_e32 v56, s100, v56
	v_ashrrev_i32_e32 v57, 31, v56
	v_lshl_add_u64 v[56:57], s[16:17], 0, v[56:57]
	v_lshlrev_b64 v[56:57], 10, v[56:57]
	v_lshl_add_u64 v[56:57], s[14:15], 0, v[56:57]
	s_lshl_b32 s100, s23, 7
	s_mov_b32 s101, 0
	v_lshl_add_u64 v[56:57], v[56:57], 0, s[100:101]
	v_lshrrev_b32_e32 v58, 5, v234
	v_lshlrev_b32_e32 v58, 4, v58
	v_mov_b32_e32 v59, 0
	v_lshl_add_u64 v[56:57], v[56:57], 0, v[58:59]
	s_mov_b32 s100, 0x5c00000
	v_lshl_add_u64 v[58:59], v[56:57], 0, s[100:101]
	s_mov_b32 s100, 0x5c08000
	v_lshl_add_u64 v[56:57], v[56:57], 0, s[100:101]
	global_load_dwordx4 v[60:63], v[58:59], off
	global_load_dwordx4 v[64:67], v[56:57], off
	global_load_dwordx4 v[68:71], v[58:59], off offset:32
	global_load_dwordx4 v[72:75], v[56:57], off offset:32
	global_load_dwordx4 v[76:79], v[58:59], off offset:64
	global_load_dwordx4 v[80:83], v[56:57], off offset:64
	global_load_dwordx4 v[84:87], v[58:59], off offset:96
	global_load_dwordx4 v[88:91], v[56:57], off offset:96
	v_cmp_lt_i32_e32 vcc, v5, v9
	v_add_u32_e32 v10, -2, v234
	v_readfirstlane_b32 s5, v8
	v_cndmask_b32_e32 v5, v5, v234, vcc
	v_lshlrev_b32_e32 v11, 2, v5
	v_cmp_lt_i32_e32 vcc, v10, v9
	s_ashr_i32 s4, s5, 6
	s_waitcnt vmcnt(8)
	v_add_f32_e32 v5, v4, v0
	v_add_f32_e32 v6, v3, v5
	v_add_f32_e32 v7, v7, v6
	ds_bpermute_b32 v0, v11, v7
	v_cndmask_b32_e32 v3, v10, v234, vcc
	v_and_b32_e32 v10, 63, v8
	v_cmp_eq_u32_e32 vcc, 0, v10
	v_lshlrev_b32_e32 v3, 2, v3
	s_waitcnt lgkmcnt(0)
	v_add_f32_e32 v0, v7, v0
	v_cndmask_b32_e32 v0, v0, v7, vcc
	ds_bpermute_b32 v3, v3, v0
	v_add_u32_e32 v11, -4, v234
	v_cmp_lt_i32_e32 vcc, v11, v9
	s_waitcnt lgkmcnt(0)
	v_add_f32_e32 v3, v0, v3
	v_cndmask_b32_e32 v11, v11, v234, vcc
	v_cmp_gt_u32_e32 vcc, 2, v10
	v_lshlrev_b32_e32 v11, 2, v11
	s_nop 0
	v_cndmask_b32_e32 v0, v3, v0, vcc
	ds_bpermute_b32 v3, v11, v0
	v_add_u32_e32 v11, -8, v234
	v_cmp_lt_i32_e32 vcc, v11, v9
	s_waitcnt lgkmcnt(0)
	v_add_f32_e32 v3, v0, v3
	v_cndmask_b32_e32 v11, v11, v234, vcc
	v_cmp_gt_u32_e32 vcc, 4, v10
	v_lshlrev_b32_e32 v11, 2, v11
	s_nop 0
	v_cndmask_b32_e32 v0, v3, v0, vcc
	ds_bpermute_b32 v3, v11, v0
	v_add_u32_e32 v11, -16, v234
	v_cmp_lt_i32_e32 vcc, v11, v9
	s_waitcnt lgkmcnt(0)
	v_add_f32_e32 v3, v0, v3
	v_cndmask_b32_e32 v11, v11, v234, vcc
	v_cmp_gt_u32_e32 vcc, 8, v10
	v_lshlrev_b32_e32 v11, 2, v11
	s_nop 0
	v_cndmask_b32_e32 v0, v3, v0, vcc
	ds_bpermute_b32 v3, v11, v0
	v_subrev_u32_e32 v11, 32, v234
	v_cmp_lt_i32_e32 vcc, v11, v9
	s_waitcnt lgkmcnt(0)
	v_add_f32_e32 v3, v0, v3
	v_cndmask_b32_e32 v11, v11, v234, vcc
	v_cmp_gt_u32_e32 vcc, 16, v10
	v_lshlrev_b32_e32 v11, 2, v11
	s_nop 0
	v_cndmask_b32_e32 v0, v3, v0, vcc
	ds_bpermute_b32 v3, v11, v0
	v_cmp_eq_u32_e32 vcc, 63, v10
	s_waitcnt lgkmcnt(0)
	v_add_f32_e32 v11, v0, v3
	s_and_saveexec_b64 s[8:9], vcc
	s_lshl_b32 s10, s4, 2
	s_add_i32 s10, s10, 0
	v_mov_b32_e32 v3, s10
	ds_write_b32 v3, v11 offset:45056
	s_or_b64 exec, exec, s[8:9]
	s_load_dwordx4 s[8:11], s[6:7], 0x20
	s_cmp_lt_i32 s4, 1
	v_mov_b32_e32 v12, 0
	s_waitcnt lgkmcnt(0)
	s_barrier
	s_cbranch_scc1 .LBB0_406
	s_mov_b32 s6, s4
	v_readlane_b32 s7, v254, 60

.LBB0_456:
	s_setprio 0
	s_mov_b64 s[16:17], s[0:1]
	s_load_dwordx2 s[10:11], s[16:17], 0xd0
	v_mbcnt_lo_u32_b32 v0, -1, 0
	v_mbcnt_hi_u32_b32 v0, -1, v0
	v_mov_b32_e32 v5, v1
	v_add_u32_e32 v87, s67, v0
	s_waitcnt lgkmcnt(0)
	s_add_u32 s14, s10, 0xbc00000
	v_bfe_u32 v0, v87, 3, 3
	v_readfirstlane_b32 s4, v87
	v_lshl_add_u64 v[2:3], s[8:9], 0, v[0:1]
	s_addc_u32 s15, s11, 0
	s_and_b32 s6, s4, 0xffffffc0
	v_lshlrev_b64 v[2:3], 11, v[2:3]
	v_and_b32_e32 v144, 7, v87
	s_ashr_i32 s7, s6, 31
	v_lshl_add_u64 v[2:3], s[14:15], 0, v[2:3]
	v_lshlrev_b32_e32 v4, 4, v144
	v_lshl_add_u64 v[2:3], s[6:7], 1, v[2:3]
	v_lshl_add_u64 v[2:3], v[2:3], 0, v[4:5]
	s_mov_b32 s5, 0xfffc5000
	v_add_co_u32_e32 v4, vcc, s5, v2
	s_mov_b32 s5, 0xfffc9000
	s_nop 0
	v_addc_co_u32_e32 v5, vcc, -1, v3, vcc
	global_load_dwordx4 v[62:65], v[4:5], off offset:-3072
	v_add_co_u32_e32 v4, vcc, s5, v2
	s_mov_b32 s5, 0xfffcd000
	s_nop 0
	v_addc_co_u32_e32 v5, vcc, -1, v3, vcc
	v_add_co_u32_e32 v6, vcc, s5, v2
	s_mov_b32 s5, 0xfffd1000
	s_nop 0
	v_addc_co_u32_e32 v7, vcc, -1, v3, vcc
	global_load_dwordx4 v[58:61], v[4:5], off offset:-3072
	global_load_dwordx4 v[54:57], v[6:7], off offset:-3072
	v_add_co_u32_e32 v4, vcc, s5, v2
	s_mov_b32 s5, 0xfffd5000
	s_nop 0
	v_addc_co_u32_e32 v5, vcc, -1, v3, vcc
	v_add_co_u32_e32 v6, vcc, s5, v2
	s_mov_b32 s5, 0xfffd9000
	s_nop 0
	v_addc_co_u32_e32 v7, vcc, -1, v3, vcc
	global_load_dwordx4 v[50:53], v[4:5], off offset:-3072
	global_load_dwordx4 v[46:49], v[6:7], off offset:-3072
	v_add_co_u32_e32 v4, vcc, s5, v2
	s_mov_b32 s5, 0xfffdd000
	s_nop 0
	v_addc_co_u32_e32 v5, vcc, -1, v3, vcc
	v_add_co_u32_e32 v6, vcc, s5, v2
	s_mov_b32 s5, 0xfffe1000
	s_nop 0
	v_addc_co_u32_e32 v7, vcc, -1, v3, vcc
	global_load_dwordx4 v[42:45], v[4:5], off offset:-3072
	global_load_dwordx4 v[38:41], v[6:7], off offset:-3072
	v_add_co_u32_e32 v4, vcc, s5, v2
	s_mov_b32 s5, 0xfffe5000
	s_nop 0
	v_addc_co_u32_e32 v5, vcc, -1, v3, vcc
	v_add_co_u32_e32 v6, vcc, s5, v2
	s_mov_b32 s5, 0xfffe9000
	s_nop 0
	v_addc_co_u32_e32 v7, vcc, -1, v3, vcc
	global_load_dwordx4 v[34:37], v[4:5], off offset:-3072
	global_load_dwordx4 v[30:33], v[6:7], off offset:-3072
	v_add_co_u32_e32 v4, vcc, s5, v2
	s_mov_b32 s5, 0xfffed000
	s_nop 0
	v_addc_co_u32_e32 v5, vcc, -1, v3, vcc
	v_add_co_u32_e32 v6, vcc, s5, v2
	s_mov_b32 s5, 0xffff1000
	s_nop 0
	v_addc_co_u32_e32 v7, vcc, -1, v3, vcc
	global_load_dwordx4 v[26:29], v[4:5], off offset:-3072
	global_load_dwordx4 v[22:25], v[6:7], off offset:-3072
	v_add_co_u32_e32 v4, vcc, s5, v2
	s_mov_b32 s5, 0xffff5000
	s_nop 0
	v_addc_co_u32_e32 v5, vcc, -1, v3, vcc
	v_add_co_u32_e32 v6, vcc, s5, v2
	s_movk_i32 s5, 0x9000
	s_nop 0
	v_addc_co_u32_e32 v7, vcc, -1, v3, vcc
	global_load_dwordx4 v[18:21], v[4:5], off offset:-3072
	global_load_dwordx4 v[14:17], v[6:7], off offset:-3072
	v_add_co_u32_e32 v4, vcc, s5, v2
	s_movk_i32 s5, 0xd000
	s_nop 0
	v_addc_co_u32_e32 v5, vcc, -1, v3, vcc
	v_add_co_u32_e32 v6, vcc, s5, v2
	v_and_b32_e32 v67, 64, v234
	s_nop 0
	v_addc_co_u32_e32 v7, vcc, -1, v3, vcc
	global_load_dwordx4 v[10:13], v[4:5], off offset:-3072
	s_nop 0
	global_load_dwordx4 v[6:9], v[6:7], off offset:-3072
	s_nop 0
	global_load_dwordx4 v[2:5], v[2:3], off offset:1024
	v_xor_b32_e32 v66, 1, v234
	v_add_u32_e32 v104, 64, v67
	s_waitcnt vmcnt(0)
	v_and_b32_e32 v151, 0xffff0000, v62
	v_and_b32_e32 v153, 0xffff0000, v63
	v_lshlrev_b32_e32 v152, 16, v62
	v_mul_f32_e32 v62, v151, v151
	v_lshlrev_b32_e32 v154, 16, v63
	v_mul_f32_e32 v63, v153, v153
	v_fmac_f32_e32 v62, v152, v152
	v_fmac_f32_e32 v63, v154, v154
	v_and_b32_e32 v155, 0xffff0000, v64
	v_add_f32_e32 v62, v62, v63
	v_lshlrev_b32_e32 v156, 16, v64
	v_mul_f32_e32 v63, v155, v155
	v_fmac_f32_e32 v63, v156, v156
	v_and_b32_e32 v157, 0xffff0000, v65
	v_cmp_lt_i32_e32 vcc, v66, v104
	v_add_f32_e32 v62, v63, v62
	v_lshlrev_b32_e32 v158, 16, v65
	v_mul_f32_e32 v63, v157, v157
	v_cndmask_b32_e32 v66, v234, v66, vcc
	v_fmac_f32_e32 v63, v158, v158
	v_lshlrev_b32_e32 v102, 2, v66
	v_add_f32_e32 v62, v63, v62
	s_nop 1
	v_add_f32_dpp v62, v62, v62 quad_perm:[1,0,3,2] row_mask:0xf bank_mask:0xf
	s_nop 1
	v_add_f32_dpp v62, v62, v62 quad_perm:[2,3,0,1] row_mask:0xf bank_mask:0xf
	s_nop 1
	v_mov_b32_e32 v63, v62
	s_nop 1
	v_add_f32_dpp v62, v63, v62 row_shl:4 row_mask:0xf bank_mask:0x5
	s_nop 1
	v_add_f32_dpp v62, v63, v62 row_shr:4 row_mask:0xf bank_mask:0xa
	s_nop 1
	v_mov_b32_e32 v63, 0
	v_xor_b32_e32 v66, 2, v234
	v_cmp_lt_i32_e32 vcc, v66, v104
	s_ashr_i32 s12, s4, 6
	s_lshl_b32 s4, s12, 2
	v_cndmask_b32_e32 v64, v234, v66, vcc
	v_lshlrev_b32_e32 v101, 2, v64
	s_waitcnt lgkmcnt(0)
	v_add_f32_e32 v62, v62, v63
	v_mov_b32_e32 v63, 0
	v_xor_b32_e32 v64, 4, v234
	v_cmp_lt_i32_e32 vcc, v64, v104
	s_add_i32 s4, s4, 0
	s_add_i32 s4, s4, 0x22000
	v_cndmask_b32_e32 v64, v234, v64, vcc
	v_lshlrev_b32_e32 v100, 2, v64
	s_waitcnt lgkmcnt(0)
	v_add_f32_e32 v62, v62, v63
	v_mov_b32_e32 v63, 0
	v_and_b32_e32 v64, 56, v87
	v_cmp_eq_u32_e32 vcc, 0, v144
	v_lshl_add_u32 v103, v64, 2, s4
	s_and_saveexec_b64 s[18:19], vcc
	s_cbranch_execz .LBB0_458
	s_waitcnt lgkmcnt(0)
	v_add_f32_e32 v62, v62, v63
	ds_write_b32 v103, v62
